# grid barrier: the acquire invalidate moved to wave 1 at barrier entry (all loads of the workgroup are complete and none follow before the closing barrier), overlapping wave 0's arrival protocol; no in
# speedup vs baseline: 1.0189x; 1.0027x over previous
.LBB0_59:
	s_cmp_gt_i32 s91, 1
	s_cselect_b64 s[2:3], -1, 0
	s_and_b64 s[0:1], s[14:15], s[2:3]
	s_andn2_b64 vcc, exec, s[0:1]
	s_cbranch_vccnz .LBB0_113
	s_waitcnt vmcnt(0)
	s_waitcnt lgkmcnt(0)
	s_barrier
	v_readlane_b32 s4, v253, 9
	s_cmp_lg_u32 s4, 64
	s_cbranch_scc1 .Lxinvw_0
	buffer_inv sc1
	s_waitcnt vmcnt(0)
.Lxinvw_0:
	s_mov_b64 s[0:1], exec
	v_readlane_b32 s4, v253, 15
	v_readlane_b32 s5, v253, 16
	s_and_b64 s[4:5], s[0:1], s[4:5]
	s_mov_b64 exec, s[4:5]
	s_cbranch_execz .LBB0_112
	s_add_i32 s4, 0, 0x27fc0
	v_mov_b32_e32 v0, s4
	s_waitcnt vmcnt(0) expcnt(0) lgkmcnt(0)
	ds_read_b32 v2, v0
	s_add_i32 s4, 0, 0x27fc4
	v_mov_b32_e32 v0, s4
	ds_read_b32 v0, v0
	s_waitcnt lgkmcnt(1)
	v_cmp_ne_u32_e32 vcc, 0, v2
	s_cbranch_vccnz .LBB0_76
	v_readlane_b32 s4, v253, 10
	v_readlane_b32 s5, v253, 11
	v_readlane_b32 s6, v253, 8
	s_mul_i32 s31, s5, s6
	s_mul_i32 s31, s31, s4
	s_add_u32 s4, s88, 0x80200
	s_addc_u32 s5, s89, 0
	s_add_u32 s6, s88, 0x80400
	s_addc_u32 s7, s89, 0
	s_add_u32 s8, s88, 0x80500
	s_addc_u32 s9, s89, 0
	s_add_u32 s10, s88, 0x80600
	s_addc_u32 s11, s89, 0
	s_add_u32 s12, s88, 0x80700
	s_addc_u32 s13, s89, 0
	s_add_u32 s14, s88, 0x80800
	s_addc_u32 s15, s89, 0
	s_add_u32 s16, s88, 0x80900
	s_addc_u32 s17, s89, 0
	s_add_u32 s18, s88, 0x80a00
	s_addc_u32 s19, s89, 0
	s_add_u32 s20, s88, 0x80b00
	s_addc_u32 s21, s89, 0
	s_add_u32 s22, s88, 0x80c00
	s_addc_u32 s23, s89, 0
	s_add_u32 s24, s88, 0x80d00
	s_addc_u32 s25, s89, 0
	s_add_u32 s26, s88, 0x80e00
	s_addc_u32 s27, s89, 0
	s_add_u32 s28, s88, 0x80f00
	s_addc_u32 s29, s89, 0
	s_add_u32 s34, s88, 0x81000
	s_addc_u32 s35, s89, 0
	s_add_u32 s40, s88, 0x81100
	s_addc_u32 s41, s89, 0
	s_add_u32 s44, s88, 0x81200
	s_addc_u32 s45, s89, 0
	s_add_u32 s52, s88, 0x81300
	s_addc_u32 s53, s89, 0
	s_mov_b32 s33, 1
	v_mov_b32_e32 v16, 0
	s_branch .LBB0_64

.LBB0_130:
	s_cmp_gt_i32 s91, 2
	s_cselect_b64 s[2:3], -1, 0
	s_and_b64 s[4:5], s[4:5], s[2:3]
	s_andn2_b64 vcc, exec, s[4:5]
	s_cbranch_vccnz .LBB0_184
	s_waitcnt vmcnt(0)
	s_waitcnt lgkmcnt(0)
	s_barrier
	v_readlane_b32 s6, v253, 9
	s_cmp_lg_u32 s6, 64
	s_cbranch_scc1 .Lxinvw_1
	buffer_inv sc1
	s_waitcnt vmcnt(0)
.Lxinvw_1:
	s_mov_b64 s[4:5], exec
	v_readlane_b32 s6, v253, 15
	v_readlane_b32 s7, v253, 16
	s_and_b64 s[6:7], s[4:5], s[6:7]
	s_mov_b64 exec, s[6:7]
	s_cbranch_execz .LBB0_183
	s_add_i32 s6, 0, 0x27fc0
	v_mov_b32_e32 v0, s6
	s_waitcnt vmcnt(0) expcnt(0) lgkmcnt(0)
	ds_read_b32 v2, v0
	s_add_i32 s6, 0, 0x27fc4
	v_mov_b32_e32 v0, s6
	ds_read_b32 v0, v0
	s_waitcnt lgkmcnt(1)
	v_cmp_ne_u32_e32 vcc, 0, v2
	s_cbranch_vccnz .LBB0_147
	v_readlane_b32 s6, v253, 10
	v_readlane_b32 s7, v253, 11
	v_readlane_b32 s8, v253, 8
	s_mul_i32 s31, s7, s8
	s_mul_i32 s31, s31, s6
	s_add_u32 s6, s88, 0x80200
	s_addc_u32 s7, s89, 0
	s_add_u32 s8, s88, 0x80400
	s_addc_u32 s9, s89, 0
	s_add_u32 s10, s88, 0x80500
	s_addc_u32 s11, s89, 0
	s_add_u32 s12, s88, 0x80600
	s_addc_u32 s13, s89, 0
	s_add_u32 s14, s88, 0x80700
	s_addc_u32 s15, s89, 0
	s_add_u32 s16, s88, 0x80800
	s_addc_u32 s17, s89, 0
	s_add_u32 s18, s88, 0x80900
	s_addc_u32 s19, s89, 0
	s_add_u32 s20, s88, 0x80a00
	s_addc_u32 s21, s89, 0
	s_add_u32 s22, s88, 0x80b00
	s_addc_u32 s23, s89, 0
	s_add_u32 s24, s88, 0x80c00
	s_addc_u32 s25, s89, 0
	s_add_u32 s26, s88, 0x80d00
	s_addc_u32 s27, s89, 0
	s_add_u32 s28, s88, 0x80e00
	s_addc_u32 s29, s89, 0
	s_add_u32 s34, s88, 0x80f00
	s_addc_u32 s35, s89, 0
	s_add_u32 s40, s88, 0x81000
	s_addc_u32 s41, s89, 0
	s_add_u32 s44, s88, 0x81100
	s_addc_u32 s45, s89, 0
	s_add_u32 s52, s88, 0x81200
	s_addc_u32 s53, s89, 0
	s_add_u32 s68, s88, 0x81300
	s_addc_u32 s69, s89, 0
	s_mov_b32 s33, 1
	v_mov_b32_e32 v16, 0
	s_branch .LBB0_135

.LBB0_347:
	s_cmp_gt_i32 s91, 3
	s_cselect_b64 s[0:1], -1, 0
	s_and_b64 s[2:3], s[4:5], s[0:1]
	v_readlane_b32 s76, v253, 10
	s_andn2_b64 vcc, exec, s[2:3]
	v_readlane_b32 s77, v253, 11
	v_readlane_b32 s78, v253, 20
	s_cbranch_vccnz .LBB0_401
	s_waitcnt vmcnt(0)
	s_barrier
	v_readlane_b32 s4, v253, 9
	s_cmp_lg_u32 s4, 64
	s_cbranch_scc1 .Lxinvw_2
	buffer_inv sc1
	s_waitcnt vmcnt(0)
.Lxinvw_2:
	s_mov_b64 s[2:3], exec
	v_readlane_b32 s4, v253, 15
	v_readlane_b32 s5, v253, 16
	s_and_b64 s[4:5], s[2:3], s[4:5]
	s_mov_b64 exec, s[4:5]
	s_cbranch_execz .LBB0_400
	s_add_i32 s4, 0, 0x27fc0
	v_mov_b32_e32 v0, s4
	s_waitcnt vmcnt(0) expcnt(0) lgkmcnt(0)
	ds_read_b32 v2, v0
	s_add_i32 s4, 0, 0x27fc4
	v_mov_b32_e32 v0, s4
	ds_read_b32 v0, v0
	s_waitcnt lgkmcnt(1)
	v_cmp_ne_u32_e32 vcc, 0, v2
	s_cbranch_vccnz .LBB0_364
	v_readlane_b32 s4, v253, 8
	s_mul_i32 s31, s77, s4
	s_add_u32 s4, s88, 0x80200
	s_addc_u32 s5, s89, 0
	s_add_u32 s6, s88, 0x80400
	s_addc_u32 s7, s89, 0
	s_add_u32 s8, s88, 0x80500
	s_addc_u32 s9, s89, 0
	s_add_u32 s10, s88, 0x80600
	s_addc_u32 s11, s89, 0
	s_add_u32 s12, s88, 0x80700
	s_addc_u32 s13, s89, 0
	s_add_u32 s14, s88, 0x80800
	s_addc_u32 s15, s89, 0
	s_add_u32 s16, s88, 0x80900
	s_addc_u32 s17, s89, 0
	s_add_u32 s18, s88, 0x80a00
	s_addc_u32 s19, s89, 0
	s_add_u32 s20, s88, 0x80b00
	s_addc_u32 s21, s89, 0
	s_add_u32 s22, s88, 0x80c00
	s_addc_u32 s23, s89, 0
	s_add_u32 s24, s88, 0x80d00
	s_addc_u32 s25, s89, 0
	s_add_u32 s26, s88, 0x80e00
	s_addc_u32 s27, s89, 0
	s_add_u32 s28, s88, 0x80f00
	s_addc_u32 s29, s89, 0
	s_add_u32 s34, s88, 0x81000
	s_addc_u32 s35, s89, 0
	s_add_u32 s52, s88, 0x81100
	s_addc_u32 s53, s89, 0
	s_add_u32 s54, s88, 0x81200
	s_addc_u32 s55, s89, 0
	s_add_u32 s56, s88, 0x81300
	s_mul_i32 s31, s31, s76
	s_addc_u32 s57, s89, 0
	s_mov_b32 s33, 1
	v_mov_b32_e32 v16, 0
	s_branch .LBB0_352

.LBB0_456:
	s_cmp_gt_i32 s91, 4
	s_cselect_b64 s[2:3], -1, 0
	s_and_b64 s[0:1], s[52:53], s[2:3]
	s_andn2_b64 vcc, exec, s[0:1]
	s_cbranch_vccnz .LBB0_510
	s_waitcnt vmcnt(0)
	s_waitcnt lgkmcnt(0)
	s_barrier
	v_readlane_b32 s4, v253, 9
	s_cmp_lg_u32 s4, 64
	s_cbranch_scc1 .Lxinvw_3
	buffer_inv sc1
	s_waitcnt vmcnt(0)
.Lxinvw_3:
	s_mov_b64 s[0:1], exec
	v_readlane_b32 s4, v253, 15
	v_readlane_b32 s5, v253, 16
	s_and_b64 s[4:5], s[0:1], s[4:5]
	s_mov_b64 exec, s[4:5]
	s_cbranch_execz .LBB0_509
	s_add_i32 s4, 0, 0x27fc0
	s_waitcnt vmcnt(37)
	v_mov_b32_e32 v0, s4
	s_waitcnt vmcnt(0) expcnt(0) lgkmcnt(0)
	ds_read_b32 v2, v0
	s_add_i32 s4, 0, 0x27fc4
	v_mov_b32_e32 v0, s4
	ds_read_b32 v0, v0
	s_waitcnt lgkmcnt(1)
	v_cmp_ne_u32_e32 vcc, 0, v2
	s_cbranch_vccnz .LBB0_473
	v_readlane_b32 s4, v253, 8
	s_mul_i32 s31, s77, s4
	s_add_u32 s4, s88, 0x80200
	s_addc_u32 s5, s89, 0
	s_add_u32 s6, s88, 0x80400
	s_addc_u32 s7, s89, 0
	s_add_u32 s8, s88, 0x80500
	s_addc_u32 s9, s89, 0
	s_add_u32 s10, s88, 0x80600
	s_addc_u32 s11, s89, 0
	s_add_u32 s12, s88, 0x80700
	s_addc_u32 s13, s89, 0
	s_add_u32 s14, s88, 0x80800
	s_addc_u32 s15, s89, 0
	s_add_u32 s16, s88, 0x80900
	s_addc_u32 s17, s89, 0
	s_add_u32 s18, s88, 0x80a00
	s_addc_u32 s19, s89, 0
	s_add_u32 s20, s88, 0x80b00
	s_addc_u32 s21, s89, 0
	s_add_u32 s22, s88, 0x80c00
	s_addc_u32 s23, s89, 0
	s_add_u32 s24, s88, 0x80d00
	s_addc_u32 s25, s89, 0
	s_add_u32 s26, s88, 0x80e00
	s_addc_u32 s27, s89, 0
	s_add_u32 s28, s88, 0x80f00
	s_addc_u32 s29, s89, 0
	s_add_u32 s34, s88, 0x81000
	s_addc_u32 s35, s89, 0
	s_add_u32 s36, s88, 0x81100
	s_addc_u32 s37, s89, 0
	s_add_u32 s38, s88, 0x81200
	s_addc_u32 s39, s89, 0
	s_add_u32 s48, s88, 0x81300
	s_mul_i32 s31, s31, s76
	s_addc_u32 s49, s89, 0
	s_mov_b32 s33, 1
	v_mov_b32_e32 v16, 0
	s_branch .LBB0_461

.LBB0_518:
	s_cmp_gt_i32 s91, 5
	s_cselect_b64 s[2:3], -1, 0
	s_and_b64 s[0:1], s[0:1], s[2:3]
	s_andn2_b64 vcc, exec, s[0:1]
	s_cbranch_vccnz .LBB0_572
	s_waitcnt vmcnt(0)
	s_waitcnt lgkmcnt(0)
	s_barrier
	v_readlane_b32 s4, v253, 9
	s_cmp_lg_u32 s4, 64
	s_cbranch_scc1 .Lxinvw_4
	buffer_inv sc1
	s_waitcnt vmcnt(0)

.LBB0_599:
	s_waitcnt vmcnt(0)
	s_waitcnt lgkmcnt(0)
	s_barrier
	v_readlane_b32 s4, v253, 9
	s_cmp_lg_u32 s4, 64
	s_cbranch_scc1 .Lxinvw_5
	buffer_inv sc1
	s_waitcnt vmcnt(0)
.Lxinvw_5:
	s_mov_b64 s[0:1], exec
	v_readlane_b32 s4, v253, 15
	v_readlane_b32 s5, v253, 16
	s_and_b64 s[4:5], s[0:1], s[4:5]
	s_mov_b64 exec, s[4:5]
	s_cbranch_execz .LBB0_651
	s_add_i32 s4, 0, 0x27fc0
	v_mov_b32_e32 v0, s4
	s_waitcnt vmcnt(0) expcnt(0) lgkmcnt(0)
	ds_read_b32 v2, v0
	s_add_i32 s4, 0, 0x27fc4
	v_mov_b32_e32 v0, s4
	ds_read_b32 v0, v0
	s_waitcnt lgkmcnt(1)
	v_cmp_ne_u32_e32 vcc, 0, v2
	s_cbranch_vccnz .LBB0_615
	v_readlane_b32 s4, v253, 8
	s_mul_i32 s31, s77, s4
	s_add_u32 s4, s88, 0x80200
	s_addc_u32 s5, s89, 0
	s_add_u32 s6, s88, 0x80400
	s_addc_u32 s7, s89, 0
	s_add_u32 s8, s88, 0x80500
	s_addc_u32 s9, s89, 0
	s_add_u32 s12, s88, 0x80600
	s_addc_u32 s13, s89, 0
	s_add_u32 s14, s88, 0x80700
	s_addc_u32 s15, s89, 0
	s_add_u32 s16, s88, 0x80800
	s_addc_u32 s17, s89, 0
	s_add_u32 s18, s88, 0x80900
	s_addc_u32 s19, s89, 0
	s_add_u32 s20, s88, 0x80a00
	s_addc_u32 s21, s89, 0
	s_add_u32 s22, s88, 0x80b00
	s_addc_u32 s23, s89, 0
	s_add_u32 s24, s88, 0x80c00
	s_addc_u32 s25, s89, 0
	s_add_u32 s26, s88, 0x80d00
	s_addc_u32 s27, s89, 0
	s_add_u32 s28, s88, 0x80e00
	s_addc_u32 s29, s89, 0
	s_add_u32 s34, s88, 0x80f00
	s_addc_u32 s35, s89, 0
	s_add_u32 s36, s88, 0x81000
	s_addc_u32 s37, s89, 0
	s_add_u32 s38, s88, 0x81100
	s_addc_u32 s39, s89, 0
	s_add_u32 s44, s88, 0x81200
	s_addc_u32 s45, s89, 0
	s_add_u32 s48, s88, 0x81300
	s_mul_i32 s31, s31, s76
	s_addc_u32 s49, s89, 0
	s_mov_b32 s33, 1
	v_mov_b32_e32 v16, 0
	s_branch .LBB0_603

.LBB0_663:
	s_cmp_gt_i32 s91, 7
	s_cselect_b64 s[0:1], -1, 0
	s_and_b64 s[2:3], s[10:11], s[0:1]
	s_andn2_b64 vcc, exec, s[2:3]
	s_cbranch_vccnz .LBB0_717
	s_waitcnt vmcnt(0)
	s_waitcnt lgkmcnt(0)
	s_barrier
	v_readlane_b32 s4, v253, 9
	s_cmp_lg_u32 s4, 64
	s_cbranch_scc1 .Lxinvw_6
	buffer_inv sc1
	s_waitcnt vmcnt(0)
.Lxinvw_6:
	s_mov_b64 s[2:3], exec
	v_readlane_b32 s4, v253, 15
	v_readlane_b32 s5, v253, 16
	s_and_b64 s[4:5], s[2:3], s[4:5]
	s_mov_b64 exec, s[4:5]
	s_cbranch_execz .LBB0_716
	s_add_i32 s4, 0, 0x27fc0
	v_mov_b32_e32 v0, s4
	s_waitcnt vmcnt(0) expcnt(0) lgkmcnt(0)
	ds_read_b32 v2, v0
	s_add_i32 s4, 0, 0x27fc4
	v_mov_b32_e32 v0, s4
	ds_read_b32 v0, v0
	s_waitcnt lgkmcnt(1)
	v_cmp_ne_u32_e32 vcc, 0, v2
	s_cbranch_vccnz .LBB0_680
	v_readlane_b32 s4, v253, 8
	s_mul_i32 s31, s77, s4
	s_add_u32 s4, s88, 0x80200
	s_addc_u32 s5, s89, 0
	s_add_u32 s6, s88, 0x80400
	s_addc_u32 s7, s89, 0
	s_add_u32 s8, s88, 0x80500
	s_addc_u32 s9, s89, 0
	s_add_u32 s10, s88, 0x80600
	s_addc_u32 s11, s89, 0
	s_add_u32 s14, s88, 0x80700
	s_addc_u32 s15, s89, 0
	s_add_u32 s16, s88, 0x80800
	s_addc_u32 s17, s89, 0
	s_add_u32 s18, s88, 0x80900
	s_addc_u32 s19, s89, 0
	s_add_u32 s20, s88, 0x80a00
	s_addc_u32 s21, s89, 0
	s_add_u32 s22, s88, 0x80b00
	s_addc_u32 s23, s89, 0
	s_add_u32 s24, s88, 0x80c00
	s_addc_u32 s25, s89, 0
	s_add_u32 s26, s88, 0x80d00
	s_addc_u32 s27, s89, 0
	s_add_u32 s28, s88, 0x80e00
	s_addc_u32 s29, s89, 0
	s_add_u32 s34, s88, 0x80f00
	s_addc_u32 s35, s89, 0
	s_add_u32 s36, s88, 0x81000
	s_addc_u32 s37, s89, 0
	s_add_u32 s38, s88, 0x81100
	s_addc_u32 s39, s89, 0
	s_add_u32 s42, s88, 0x81200
	s_addc_u32 s43, s89, 0
	s_add_u32 s44, s88, 0x81300
	s_mul_i32 s31, s31, s76
	s_addc_u32 s45, s89, 0
	s_mov_b32 s33, 1
	v_mov_b32_e32 v16, 0
	s_branch .LBB0_668

.LBB0_743:
	s_cmp_gt_i32 s91, 8
	s_cselect_b64 s[2:3], -1, 0
	s_and_b64 s[0:1], s[8:9], s[2:3]
	s_andn2_b64 vcc, exec, s[0:1]
	s_cbranch_vccnz .LBB0_797
	s_waitcnt vmcnt(0)
	s_waitcnt lgkmcnt(0)
	s_barrier
	v_readlane_b32 s4, v253, 9
	s_cmp_lg_u32 s4, 64
	s_cbranch_scc1 .Lxinvw_7
	buffer_inv sc1
	s_waitcnt vmcnt(0)
.Lxinvw_7:
	s_mov_b64 s[0:1], exec
	v_readlane_b32 s4, v253, 15
	v_readlane_b32 s5, v253, 16
	s_and_b64 s[4:5], s[0:1], s[4:5]
	s_mov_b64 exec, s[4:5]
	s_cbranch_execz .LBB0_796
	s_add_i32 s4, 0, 0x27fc0
	v_mov_b32_e32 v0, s4
	s_waitcnt vmcnt(0) expcnt(0) lgkmcnt(0)
	ds_read_b32 v2, v0
	s_add_i32 s4, 0, 0x27fc4
	v_mov_b32_e32 v0, s4
	ds_read_b32 v0, v0
	s_waitcnt lgkmcnt(1)
	v_cmp_ne_u32_e32 vcc, 0, v2
	s_cbranch_vccnz .LBB0_760
	v_readlane_b32 s4, v253, 8
	s_mul_i32 s31, s77, s4
	s_add_u32 s4, s88, 0x80200
	s_addc_u32 s5, s89, 0
	s_add_u32 s8, s88, 0x80400
	s_addc_u32 s9, s89, 0
	s_add_u32 s10, s88, 0x80500
	s_addc_u32 s11, s89, 0
	s_add_u32 s12, s88, 0x80600
	s_addc_u32 s13, s89, 0
	s_add_u32 s14, s88, 0x80700
	s_addc_u32 s15, s89, 0
	s_add_u32 s16, s88, 0x80800
	s_addc_u32 s17, s89, 0
	s_add_u32 s18, s88, 0x80900
	s_addc_u32 s19, s89, 0
	s_add_u32 s20, s88, 0x80a00
	s_addc_u32 s21, s89, 0
	s_add_u32 s22, s88, 0x80b00
	s_addc_u32 s23, s89, 0
	s_add_u32 s24, s88, 0x80c00
	s_addc_u32 s25, s89, 0
	s_add_u32 s26, s88, 0x80d00
	s_addc_u32 s27, s89, 0
	s_add_u32 s28, s88, 0x80e00
	s_addc_u32 s29, s89, 0
	s_add_u32 s34, s88, 0x80f00
	s_addc_u32 s35, s89, 0
	s_add_u32 s36, s88, 0x81000
	s_addc_u32 s37, s89, 0
	s_add_u32 s38, s88, 0x81100
	s_addc_u32 s39, s89, 0
	s_add_u32 s42, s88, 0x81200
	s_addc_u32 s43, s89, 0
	s_add_u32 s44, s88, 0x81300
	s_mul_i32 s31, s31, s76
	s_addc_u32 s45, s89, 0
	s_mov_b32 s33, 1
	v_mov_b32_e32 v16, 0
	s_branch .LBB0_748

.LBB0_863:
	s_cmp_gt_i32 s91, 9
	s_cselect_b64 s[2:3], -1, 0
	s_and_b64 s[0:1], s[0:1], s[2:3]
	s_andn2_b64 vcc, exec, s[0:1]
	s_cbranch_vccnz .LBB0_917
	s_waitcnt vmcnt(0)
	s_waitcnt vmcnt(0) lgkmcnt(0)
	s_barrier
	v_readlane_b32 s4, v253, 9
	s_cmp_lg_u32 s4, 64
	s_cbranch_scc1 .Lxinvw_8
	buffer_inv sc1
	s_waitcnt vmcnt(0)

.LBB0_959:
	s_cmp_gt_i32 s91, 10
	s_cselect_b64 s[2:3], -1, 0
	s_and_b64 s[0:1], s[0:1], s[2:3]
	s_andn2_b64 vcc, exec, s[0:1]
	s_cbranch_vccnz .LBB0_1013
	s_waitcnt vmcnt(0)
	s_waitcnt vmcnt(0) lgkmcnt(0)
	s_barrier
	v_readlane_b32 s4, v253, 9
	s_cmp_lg_u32 s4, 64
	s_cbranch_scc1 .Lxinvw_9
	buffer_inv sc1
	s_waitcnt vmcnt(0)
.Lxinvw_9:
	s_mov_b64 s[0:1], exec
	v_readlane_b32 s4, v253, 15
	v_readlane_b32 s5, v253, 16
	s_and_b64 s[4:5], s[0:1], s[4:5]
	s_mov_b64 exec, s[4:5]
	s_cbranch_execz .LBB0_1012
	s_add_i32 s4, 0, 0x27fc0
	v_mov_b32_e32 v0, s4
	s_waitcnt vmcnt(0) expcnt(0) lgkmcnt(0)
	ds_read_b32 v2, v0
	s_add_i32 s4, 0, 0x27fc4
	v_mov_b32_e32 v0, s4
	ds_read_b32 v0, v0
	s_waitcnt lgkmcnt(1)
	v_cmp_ne_u32_e32 vcc, 0, v2
	s_cbranch_vccnz .LBB0_976
	v_readlane_b32 s4, v253, 8
	s_mul_i32 s31, s77, s4
	s_add_u32 s4, s88, 0x80200
	s_addc_u32 s5, s89, 0
	s_add_u32 s6, s88, 0x80400
	s_addc_u32 s7, s89, 0
	s_add_u32 s8, s88, 0x80500
	s_addc_u32 s9, s89, 0
	s_add_u32 s10, s88, 0x80600
	s_addc_u32 s11, s89, 0
	s_add_u32 s12, s88, 0x80700
	s_addc_u32 s13, s89, 0
	s_add_u32 s14, s88, 0x80800
	s_addc_u32 s15, s89, 0
	s_add_u32 s16, s88, 0x80900
	s_addc_u32 s17, s89, 0
	s_add_u32 s18, s88, 0x80a00
	s_addc_u32 s19, s89, 0
	s_add_u32 s20, s88, 0x80b00
	s_addc_u32 s21, s89, 0
	s_add_u32 s22, s88, 0x80c00
	s_addc_u32 s23, s89, 0
	s_add_u32 s24, s88, 0x80d00
	s_addc_u32 s25, s89, 0
	s_add_u32 s26, s88, 0x80e00
	s_addc_u32 s27, s89, 0
	s_add_u32 s28, s88, 0x80f00
	s_addc_u32 s29, s89, 0
	s_add_u32 s34, s88, 0x81000
	s_addc_u32 s35, s89, 0
	s_add_u32 s36, s88, 0x81100
	s_addc_u32 s37, s89, 0
	s_add_u32 s38, s88, 0x81200
	s_addc_u32 s39, s89, 0
	s_add_u32 s42, s88, 0x81300
	s_mul_i32 s31, s31, s76
	s_addc_u32 s43, s89, 0
	s_mov_b32 s33, 1
	v_mov_b32_e32 v16, 0
	s_branch .LBB0_964

.LBB0_1019:
	s_cmp_gt_i32 s91, 11
	s_cselect_b64 s[2:3], -1, 0
	s_and_b64 s[0:1], s[4:5], s[2:3]
	s_andn2_b64 vcc, exec, s[0:1]
	s_cbranch_vccnz .LBB0_1073
	s_waitcnt vmcnt(0)
	s_waitcnt vmcnt(0) lgkmcnt(0)
	s_barrier
	v_readlane_b32 s4, v253, 9
	s_cmp_lg_u32 s4, 64
	s_cbranch_scc1 .Lxinvw_10
	buffer_inv sc1
	s_waitcnt vmcnt(0)

.LBB0_1112:
	s_cmp_gt_i32 s91, 12
	s_cselect_b64 s[2:3], -1, 0
	s_and_b64 s[4:5], s[6:7], s[2:3]
	s_andn2_b64 vcc, exec, s[4:5]
	s_cbranch_vccnz .LBB0_1166
	s_waitcnt vmcnt(0)
	s_waitcnt vmcnt(0) lgkmcnt(0)
	s_barrier
	v_readlane_b32 s6, v253, 9
	s_cmp_lg_u32 s6, 64
	s_cbranch_scc1 .Lxinvw_11
	buffer_inv sc1
	s_waitcnt vmcnt(0)
.Lxinvw_11:
	s_mov_b64 s[4:5], exec
	v_readlane_b32 s6, v253, 15
	v_readlane_b32 s7, v253, 16
	s_and_b64 s[6:7], s[4:5], s[6:7]
	s_mov_b64 exec, s[6:7]
	s_cbranch_execz .LBB0_1165
	s_add_i32 s6, 0, 0x27fc0
	v_mov_b32_e32 v0, s6
	s_waitcnt vmcnt(0) expcnt(0) lgkmcnt(0)
	ds_read_b32 v2, v0
	s_add_i32 s6, 0, 0x27fc4
	v_mov_b32_e32 v0, s6
	ds_read_b32 v0, v0
	s_waitcnt lgkmcnt(1)
	v_cmp_ne_u32_e32 vcc, 0, v2
	s_cbranch_vccnz .LBB0_1129
	v_readlane_b32 s6, v253, 8
	s_mul_i32 s31, s77, s6
	s_add_u32 s6, s88, 0x80200
	s_addc_u32 s7, s89, 0
	s_add_u32 s8, s88, 0x80400
	s_addc_u32 s9, s89, 0
	s_add_u32 s10, s88, 0x80500
	s_addc_u32 s11, s89, 0
	s_add_u32 s12, s88, 0x80600
	s_addc_u32 s13, s89, 0
	s_add_u32 s14, s88, 0x80700
	s_addc_u32 s15, s89, 0
	s_add_u32 s16, s88, 0x80800
	s_addc_u32 s17, s89, 0
	s_add_u32 s18, s88, 0x80900
	s_addc_u32 s19, s89, 0
	s_add_u32 s20, s88, 0x80a00
	s_addc_u32 s21, s89, 0
	s_add_u32 s22, s88, 0x80b00
	s_addc_u32 s23, s89, 0
	s_add_u32 s24, s88, 0x80c00
	s_addc_u32 s25, s89, 0
	s_add_u32 s26, s88, 0x80d00
	s_addc_u32 s27, s89, 0
	s_add_u32 s28, s88, 0x80e00
	s_addc_u32 s29, s89, 0
	s_add_u32 s34, s88, 0x80f00
	s_addc_u32 s35, s89, 0
	s_add_u32 s36, s88, 0x81000
	s_addc_u32 s37, s89, 0
	s_add_u32 s38, s88, 0x81100
	s_addc_u32 s39, s89, 0
	s_add_u32 s42, s88, 0x81200
	s_addc_u32 s43, s89, 0
	s_add_u32 s44, s88, 0x81300
	s_mul_i32 s31, s31, s76
	s_addc_u32 s45, s89, 0
	s_mov_b32 s33, 1
	v_mov_b32_e32 v16, 0
	s_branch .LBB0_1117
